# baseline (speedup 1.0000x reference)
_Z12giou_partialPK15HIP_vector_typeIfLj4EES2_S2_PKiPS_IfLj2EE:
	s_load_dwordx8 s[16:23], s[0:1], 0x0
	s_load_dwordx2 s[24:25], s[0:1], 0x20
	s_cmpk_ge_u32 s2, 0x100
	s_cbranch_scc1 .Llate_block
	s_movk_i32 s3, 0x200
	s_lshl_b32 s6, s2, 10
	v_cmp_gt_u32_e32 vcc, s3, v0
	v_lshlrev_b32_e32 v11, 4, v0
	v_lshrrev_b32_e32 v1, 6, v0
	v_and_b32_e32 v10, 63, v0
	v_lshl_add_u32 v6, v1, 18, s6
	v_lshlrev_b32_e32 v8, 2, v6
	v_lshl_add_u32 v8, v10, 4, v8
	s_lshl_b32 s7, s2, 14
	v_readfirstlane_b32 s15, v1
	v_add_u32_e32 v43, 0x200, v6
	s_waitcnt lgkmcnt(0)
	s_add_u32 s20, s20, s7
	s_addc_u32 s21, s21, 0
	global_load_dwordx4 v[12:15], v8, s[22:23] nt
	global_load_dwordx4 v[16:19], v8, s[22:23] offset:1024 nt
	global_load_dwordx4 v[26:29], v8, s[22:23] offset:2048 nt
	global_load_dwordx4 v[30:33], v8, s[22:23] offset:3072 nt
	s_and_saveexec_b64 s[8:9], vcc
	s_cbranch_execz .Lno_anc
	v_add_u32_e32 v9, 0x2000, v11
	s_lshl_b32 s4, s15, 10
	s_add_u32 m0, s4, 0x8000
	s_nop 0
	global_load_lds_dwordx4 v11, s[20:21] nt
	s_add_u32 m0, s4, 0xa000
	s_nop 0
	global_load_lds_dwordx4 v9, s[20:21] nt

.LcompB_end:
	s_or_b64 exec, exec, s[10:11]
	s_ashr_i32 s0, s14, 16
	s_add_i32 s3, s3, s0
	s_mov_b32 s28, s3
	s_waitcnt lgkmcnt(0)
	v_mov_b32_e32 v2, 0
	v_cmp_gt_i32_e32 vcc, s27, v10
	s_and_b64 exec, exec, vcc
	s_mov_b64 s[30:31], exec
	s_cbranch_execz .Lskip_issueA
	v_lshlrev_b32_e32 v3, 1, v10
	v_lshl_or_b32 v3, v1, 10, v3
	v_mov_b32_e32 v4, v10
	ds_read_u16 v5, v3
	s_waitcnt lgkmcnt(0)
	v_add_u32_e32 v8, v6, v5
	v_lshlrev_b32_e32 v8, 4, v8
	global_load_dwordx4 v[12:15], v8, s[16:17] nt
	global_load_dwordx4 v[16:19], v8, s[18:19] nt
	v_lshlrev_b32_e32 v5, 4, v5
